# baseline (speedup 1.0000x reference)
.LBB1_8:
	s_or_b64 exec, exec, s[4:5]
	v_add_u32_e32 v10, v172, v2
	s_waitcnt vmcnt(1) lgkmcnt(0)
	s_barrier
	ds_read_b128 v[18:21], v10 offset:256
	ds_read_b128 v[22:25], v10 offset:288
	ds_read_b128 v[82:85], v10 offset:320
	ds_read_b128 v[86:89], v10 offset:352
	ds_read_b128 v[74:77], v10 offset:384
	ds_read_b128 v[78:81], v10 offset:416
	ds_read_b128 v[2:5], v213 offset:32768
	ds_read_b128 v[6:9], v213 offset:0
	ds_read_b128 v[66:69], v10 offset:448
	ds_read_b128 v[70:73], v10 offset:480
	ds_read_b128 v[10:13], v213 offset:1024
	s_waitcnt lgkmcnt(3)
	v_pk_mul_f32 v[26:27], v[8:9], v[20:21]
	v_pk_mul_f32 v[28:29], v[6:7], v[18:19]
	ds_read_b128 v[14:17], v213 offset:8192
	s_waitcnt lgkmcnt(1)
	v_pk_mul_f32 v[12:13], v[12:13], v[24:25]
	v_pk_mul_f32 v[10:11], v[10:11], v[22:23]
	v_pk_fma_f32 v[30:31], v[8:9], v[20:21], v[12:13]
	v_pk_fma_f32 v[32:33], v[6:7], v[18:19], v[10:11]
	v_cvt_pk_bf16_f32 v9, v12, v13
	v_cvt_pk_bf16_f32 v7, v26, v27
	v_cvt_pk_bf16_f32 v8, v10, v11
	v_cvt_pk_bf16_f32 v6, v28, v29
	ds_read_b128 v[10:13], v213 offset:33792
	s_nop 0
	v_mfma_f32_32x32x16_bf16 v[34:49], v[2:5], v[6:9], 0
	ds_read_b128 v[6:9], v213 offset:9216
	s_waitcnt lgkmcnt(2)
	v_mul_f32_e32 v26, v16, v20
	v_mul_f32_e32 v27, v17, v21
	v_pk_mul_f32 v[50:51], v[14:15], v[18:19]
	s_mov_b32 s4, 0x3727c5ac
	s_waitcnt lgkmcnt(0)
	v_pk_mul_f32 v[8:9], v[8:9], v[24:25]
	v_pk_mul_f32 v[28:29], v[6:7], v[22:23]
	v_pk_fma_f32 v[90:91], v[16:17], v[20:21], v[8:9]
	v_pk_fma_f32 v[92:93], v[14:15], v[18:19], v[28:29]
	ds_read_b128 v[14:17], v213 offset:2048
	v_cvt_pk_bf16_f32 v9, v8, v9
	v_cvt_pk_bf16_f32 v7, v26, v27
	v_cvt_pk_bf16_f32 v8, v28, v29
	ds_read_b128 v[26:29], v213 offset:3072
	v_cvt_pk_bf16_f32 v6, v50, v51
	s_waitcnt lgkmcnt(1)
	v_pk_mul_f32 v[94:95], v[14:15], v[82:83]
	s_mov_b32 s0, 0x3c800000
	v_mfma_f32_32x32x16_bf16 v[50:65], v[2:5], v[6:9], 0
	v_mul_f32_e32 v2, v16, v84
	v_mul_f32_e32 v3, v17, v85
	s_waitcnt lgkmcnt(0)
	v_mul_f32_e32 v4, v28, v88
	v_mul_f32_e32 v5, v29, v89
	v_pk_mul_f32 v[6:7], v[26:27], v[86:87]
	v_pk_fma_f32 v[8:9], v[16:17], v[84:85], v[4:5]
	v_cvt_pk_bf16_f32 v3, v2, v3
	v_pk_fma_f32 v[14:15], v[14:15], v[82:83], v[6:7]
	v_pk_add_f32 v[26:27], v[8:9], v[30:31]
	v_cvt_pk_bf16_f32 v5, v4, v5
	v_cvt_pk_bf16_f32 v4, v6, v7
	ds_read_b128 v[6:9], v213 offset:10240
	v_pk_add_f32 v[28:29], v[14:15], v[32:33]
	ds_read_b128 v[14:17], v213 offset:11264
	v_cvt_pk_bf16_f32 v2, v94, v95
	s_waitcnt lgkmcnt(1)
	v_pk_mul_f32 v[30:31], v[6:7], v[82:83]
	v_mov_b64_e32 v[152:153], s[4:5]
	v_mfma_f32_32x32x16_bf16 v[34:49], v[10:13], v[2:5], v[34:49]
	v_mul_f32_e32 v2, v8, v84
	v_mul_f32_e32 v3, v9, v85
	s_waitcnt lgkmcnt(0)
	v_mul_f32_e32 v4, v16, v88
	v_mul_f32_e32 v5, v17, v89
	v_pk_mul_f32 v[14:15], v[14:15], v[86:87]
	v_pk_fma_f32 v[8:9], v[8:9], v[84:85], v[4:5]
	v_pk_fma_f32 v[6:7], v[6:7], v[82:83], v[14:15]
	v_cvt_pk_bf16_f32 v5, v4, v5
	v_cvt_pk_bf16_f32 v3, v2, v3
	v_cvt_pk_bf16_f32 v4, v14, v15
	v_pk_add_f32 v[32:33], v[8:9], v[90:91]
	v_pk_add_f32 v[90:91], v[6:7], v[92:93]
	ds_read_b128 v[6:9], v213 offset:34816
	ds_read_b128 v[14:17], v213 offset:4096
	v_cvt_pk_bf16_f32 v2, v30, v31
	s_mov_b32 s13, 0
	s_mov_b64 s[6:7], 0
	v_mfma_f32_32x32x16_bf16 v[50:65], v[10:13], v[2:5], v[50:65]
	ds_read_b128 v[2:5], v213 offset:5120
	ds_read_b128 v[10:13], v213 offset:12288
	s_waitcnt lgkmcnt(2)
	v_pk_mul_f32 v[30:31], v[16:17], v[76:77]
	v_pk_mul_f32 v[92:93], v[14:15], v[74:75]
	s_waitcnt lgkmcnt(1)
	v_pk_mul_f32 v[4:5], v[4:5], v[80:81]
	v_pk_mul_f32 v[94:95], v[2:3], v[78:79]
	v_pk_fma_f32 v[2:3], v[16:17], v[76:77], v[4:5]
	v_cvt_pk_bf16_f32 v5, v4, v5
	v_pk_add_f32 v[96:97], v[2:3], v[26:27]
	v_cvt_pk_bf16_f32 v3, v30, v31
	v_cvt_pk_bf16_f32 v4, v94, v95
	v_cvt_pk_bf16_f32 v2, v92, v93
	v_pk_fma_f32 v[14:15], v[14:15], v[74:75], v[94:95]
	s_waitcnt lgkmcnt(0)
	v_pk_mul_f32 v[30:31], v[10:11], v[74:75]
	v_mfma_f32_32x32x16_bf16 v[34:49], v[6:9], v[2:5], v[34:49]
	ds_read_b128 v[2:5], v213 offset:13312
	v_add_f32_e32 v98, v14, v28
	v_add_f32_e32 v99, v15, v29
	ds_read_b128 v[14:17], v213 offset:35840
	v_pk_mul_f32 v[26:27], v[12:13], v[76:77]
	s_waitcnt lgkmcnt(1)
	v_pk_mul_f32 v[4:5], v[4:5], v[80:81]
	v_pk_mul_f32 v[28:29], v[2:3], v[78:79]
	v_pk_fma_f32 v[2:3], v[12:13], v[76:77], v[4:5]
	v_pk_fma_f32 v[10:11], v[10:11], v[74:75], v[28:29]
	v_pk_add_f32 v[32:33], v[2:3], v[32:33]
	v_pk_add_f32 v[92:93], v[10:11], v[90:91]
	ds_read_b128 v[10:13], v213 offset:6144
	v_cvt_pk_bf16_f32 v5, v4, v5
	v_cvt_pk_bf16_f32 v3, v26, v27
	v_cvt_pk_bf16_f32 v4, v28, v29
	ds_read_b128 v[26:29], v213 offset:7168
	v_cvt_pk_bf16_f32 v2, v30, v31
	s_waitcnt lgkmcnt(1)
	v_pk_mul_f32 v[30:31], v[10:11], v[66:67]
	v_mfma_f32_32x32x16_bf16 v[50:65], v[6:9], v[2:5], v[50:65]
	v_mul_f32_e32 v2, v12, v68
	v_mul_f32_e32 v3, v13, v69
	s_waitcnt lgkmcnt(0)
	v_mul_f32_e32 v4, v28, v72
	v_mul_f32_e32 v5, v29, v73
	v_pk_mul_f32 v[6:7], v[26:27], v[70:71]
	v_pk_fma_f32 v[8:9], v[12:13], v[68:69], v[4:5]
	v_cvt_pk_bf16_f32 v3, v2, v3
	v_pk_fma_f32 v[10:11], v[10:11], v[66:67], v[6:7]
	v_pk_add_f32 v[94:95], v[8:9], v[96:97]
	v_cvt_pk_bf16_f32 v5, v4, v5
	v_cvt_pk_bf16_f32 v4, v6, v7
	ds_read_b128 v[6:9], v213 offset:14336
	v_pk_add_f32 v[96:97], v[10:11], v[98:99]
	ds_read_b128 v[10:13], v213 offset:15360
	v_cvt_pk_bf16_f32 v2, v30, v31
	s_waitcnt lgkmcnt(1)
	v_pk_mul_f32 v[30:31], v[6:7], v[66:67]
	v_mfma_f32_32x32x16_bf16 v[34:49], v[14:17], v[2:5], v[34:49]
	s_waitcnt lgkmcnt(0)
	v_mul_f32_e32 v10, v10, v70
	v_mul_f32_e32 v11, v11, v71
	v_mul_f32_e32 v2, v8, v68
	v_mul_f32_e32 v3, v9, v69
	v_pk_mul_f32 v[4:5], v[12:13], v[72:73]
	v_pk_fma_f32 v[6:7], v[6:7], v[66:67], v[10:11]
	v_pk_fma_f32 v[8:9], v[8:9], v[68:69], v[4:5]
	v_pk_add_f32 v[92:93], v[6:7], v[92:93]
	v_cvt_pk_bf16_f32 v3, v2, v3
	v_pk_add_f32 v[90:91], v[8:9], v[32:33]
	v_cvt_pk_bf16_f32 v5, v4, v5
	v_cvt_pk_bf16_f32 v4, v10, v11
	ds_read_b128 v[26:29], v213 offset:36864
	ds_read_b128 v[6:9], v213 offset:16384
	v_cvt_pk_bf16_f32 v2, v30, v31
	ds_read_b128 v[98:101], v213 offset:25600
	ds_read_b128 v[102:105], v213 offset:37888
	v_mfma_f32_32x32x16_bf16 v[50:65], v[14:17], v[2:5], v[50:65]
	ds_read_b128 v[2:5], v213 offset:17408
	ds_read_b128 v[30:33], v213 offset:24576
	s_waitcnt lgkmcnt(4)
	v_pk_mul_f32 v[12:13], v[6:7], v[18:19]
	v_pk_mul_f32 v[10:11], v[8:9], v[20:21]
	s_waitcnt lgkmcnt(1)
	v_pk_mul_f32 v[14:15], v[2:3], v[22:23]
	v_pk_mul_f32 v[22:23], v[98:99], v[22:23]
	v_pk_fma_f32 v[112:113], v[6:7], v[18:19], v[14:15]
	s_waitcnt lgkmcnt(0)
	v_pk_mul_f32 v[114:115], v[30:31], v[18:19]
	v_pk_fma_f32 v[118:119], v[30:31], v[18:19], v[22:23]
	v_pk_mul_f32 v[4:5], v[4:5], v[24:25]
	v_pk_mul_f32 v[106:107], v[32:33], v[20:21]
	v_pk_mul_f32 v[24:25], v[100:101], v[24:25]
	ds_read_b128 v[98:101], v213 offset:18432
	v_cvt_pk_bf16_f32 v19, v106, v107
	ds_read_b128 v[106:109], v213 offset:19456
	v_pk_fma_f32 v[110:111], v[8:9], v[20:21], v[4:5]
	v_cvt_pk_bf16_f32 v5, v4, v5
	v_cvt_pk_bf16_f32 v3, v10, v11
	v_cvt_pk_bf16_f32 v4, v14, v15
	s_waitcnt lgkmcnt(0)
	v_pk_mul_f32 v[106:107], v[106:107], v[86:87]
	v_cvt_pk_bf16_f32 v2, v12, v13
	v_pk_mul_f32 v[120:121], v[98:99], v[82:83]
	v_pk_mul_f32 v[108:109], v[108:109], v[88:89]
	v_pk_fma_f32 v[98:99], v[98:99], v[82:83], v[106:107]
	v_mfma_f32_32x32x16_bf16 v[2:17], v[26:29], v[2:5], 0
	v_cvt_pk_bf16_f32 v18, v114, v115
	v_mul_f32_e32 v114, v100, v84
	v_mul_f32_e32 v115, v101, v85
	v_fma_f32 v100, v100, v84, v108
	v_fma_f32 v101, v101, v85, v109
	v_pk_add_f32 v[124:125], v[98:99], v[112:113]
	v_pk_add_f32 v[122:123], v[100:101], v[110:111]
	v_cvt_pk_bf16_f32 v101, v108, v109
	v_cvt_pk_bf16_f32 v100, v106, v107
	ds_read_b128 v[106:109], v213 offset:26624
	v_pk_fma_f32 v[116:117], v[32:33], v[20:21], v[24:25]
	v_cvt_pk_bf16_f32 v21, v24, v25
	v_cvt_pk_bf16_f32 v20, v22, v23
	ds_read_b128 v[110:113], v213 offset:27648
	v_cvt_pk_bf16_f32 v99, v114, v115
	v_mfma_f32_32x32x16_bf16 v[18:33], v[26:29], v[18:21], 0
	v_cvt_pk_bf16_f32 v98, v120, v121
	s_waitcnt lgkmcnt(1)
	v_mul_f32_e32 v114, v106, v82
	v_mul_f32_e32 v115, v107, v83
	s_waitcnt lgkmcnt(0)
	v_pk_mul_f32 v[86:87], v[110:111], v[86:87]
	v_pk_mul_f32 v[88:89], v[112:113], v[88:89]
	v_pk_fma_f32 v[82:83], v[106:107], v[82:83], v[86:87]
	v_mfma_f32_32x32x16_bf16 v[2:17], v[102:105], v[98:101], v[2:17]
	v_mul_f32_e32 v98, v108, v84
	v_mul_f32_e32 v99, v109, v85
	v_fma_f32 v84, v108, v84, v88
	v_fma_f32 v85, v109, v85, v89
	v_add_f32_e32 v108, v82, v118
	v_add_f32_e32 v109, v83, v119
	v_cvt_pk_bf16_f32 v83, v98, v99
	v_pk_add_f32 v[106:107], v[84:85], v[116:117]
	v_cvt_pk_bf16_f32 v85, v88, v89
	v_cvt_pk_bf16_f32 v84, v86, v87
	ds_read_b128 v[86:89], v213 offset:38912
	ds_read_b128 v[98:101], v213 offset:20480
	v_cvt_pk_bf16_f32 v82, v114, v115
	s_waitcnt lgkmcnt(0)
	v_pk_mul_f32 v[110:111], v[100:101], v[76:77]
	v_mfma_f32_32x32x16_bf16 v[18:33], v[102:105], v[82:85], v[18:33]
	ds_read_b128 v[82:85], v213 offset:21504
	ds_read_b128 v[102:105], v213 offset:28672
	v_mul_f32_e32 v112, v98, v74
	v_mul_f32_e32 v113, v99, v75
	s_waitcnt lgkmcnt(1)
	v_pk_mul_f32 v[84:85], v[84:85], v[80:81]
	v_pk_mul_f32 v[114:115], v[82:83], v[78:79]
	v_pk_fma_f32 v[82:83], v[100:101], v[76:77], v[84:85]
	v_cvt_pk_bf16_f32 v85, v84, v85
	v_pk_add_f32 v[116:117], v[82:83], v[122:123]
	v_cvt_pk_bf16_f32 v83, v110, v111
	v_cvt_pk_bf16_f32 v84, v114, v115
	v_cvt_pk_bf16_f32 v82, v112, v113
	v_pk_fma_f32 v[98:99], v[98:99], v[74:75], v[114:115]
	s_waitcnt lgkmcnt(0)
	v_pk_mul_f32 v[112:113], v[102:103], v[74:75]
	v_mfma_f32_32x32x16_bf16 v[2:17], v[86:89], v[82:85], v[2:17]
	ds_read_b128 v[82:85], v213 offset:29696
	v_add_f32_e32 v118, v98, v124
	v_add_f32_e32 v119, v99, v125
	v_mul_f32_e32 v110, v104, v76
	v_mul_f32_e32 v111, v105, v77
	ds_read_b128 v[98:101], v213 offset:39936
	s_waitcnt lgkmcnt(1)
	v_pk_mul_f32 v[78:79], v[82:83], v[78:79]
	v_pk_mul_f32 v[80:81], v[84:85], v[80:81]
	v_pk_fma_f32 v[74:75], v[102:103], v[74:75], v[78:79]
	v_pk_fma_f32 v[76:77], v[104:105], v[76:77], v[80:81]
	v_pk_add_f32 v[104:105], v[74:75], v[108:109]
	v_pk_add_f32 v[102:103], v[76:77], v[106:107]
	v_cvt_pk_bf16_f32 v77, v80, v81
	v_cvt_pk_bf16_f32 v76, v78, v79
	ds_read_b128 v[78:81], v213 offset:22528
	ds_read_b128 v[82:85], v213 offset:23552
	v_cvt_pk_bf16_f32 v75, v110, v111
	v_cvt_pk_bf16_f32 v74, v112, v113
	s_waitcnt lgkmcnt(0)
	v_pk_mul_f32 v[82:83], v[82:83], v[70:71]
	v_mfma_f32_32x32x16_bf16 v[18:33], v[86:89], v[74:77], v[18:33]
	v_mul_f32_e32 v74, v80, v68
	v_mul_f32_e32 v75, v81, v69
	v_mul_f32_e32 v76, v84, v72
	v_mul_f32_e32 v77, v85, v73
	v_mul_f32_e32 v86, v78, v66
	v_mul_f32_e32 v87, v79, v67
	v_pk_fma_f32 v[80:81], v[80:81], v[68:69], v[76:77]
	v_pk_fma_f32 v[78:79], v[78:79], v[66:67], v[82:83]
	v_cvt_pk_bf16_f32 v75, v74, v75
	v_pk_add_f32 v[88:89], v[80:81], v[116:117]
	v_pk_add_f32 v[106:107], v[78:79], v[118:119]
	ds_read_b128 v[78:81], v213 offset:30720
	v_cvt_pk_bf16_f32 v77, v76, v77
	v_cvt_pk_bf16_f32 v76, v82, v83
	ds_read_b128 v[82:85], v213 offset:31744
	v_cvt_pk_bf16_f32 v74, v86, v87
	s_waitcnt lgkmcnt(0)
	v_pk_mul_f32 v[72:73], v[84:85], v[72:73]
	v_mfma_f32_32x32x16_bf16 v[2:17], v[98:101], v[74:77], v[2:17]
	v_mul_f32_e32 v74, v80, v68
	v_mul_f32_e32 v75, v81, v69
	v_fma_f32 v68, v80, v68, v72
	v_fma_f32 v69, v81, v69, v73
	v_mul_f32_e32 v70, v82, v70
	v_mul_f32_e32 v71, v83, v71
	v_pk_add_f32 v[84:85], v[68:69], v[102:103]
	v_cvt_pk_bf16_f32 v69, v72, v73
	v_add_f32_e32 v72, v97, v96
	v_add_f32_e32 v73, v94, v95
	v_pk_mul_f32 v[76:77], v[78:79], v[66:67]
	v_pk_fma_f32 v[66:67], v[78:79], v[66:67], v[70:71]
	v_add_f32_e32 v72, v72, v73
	v_pk_add_f32 v[86:87], v[66:67], v[104:105]
	v_mov_b32_e32 v66, v72
	s_nop 1
	v_permlane32_swap_b32_e32 v72, v66
	v_add_f32_e32 v66, v72, v66
	v_cvt_pk_bf16_f32 v67, v74, v75
	v_rcp_f32_e32 v74, v66
	v_cvt_pk_bf16_f32 v68, v70, v71
	v_cvt_pk_bf16_f32 v66, v76, v77
	v_pk_mul_f32 v[70:71], v[46:47], v[74:75] op_sel_hi:[1,0]
	s_nop 0
	v_mfma_f32_32x32x16_bf16 v[18:33], v[98:101], v[66:69], v[18:33]
	v_mul_f32_e32 v66, v42, v74
	v_mul_f32_e32 v67, v43, v74
	v_add_f32_e32 v42, v93, v92
	v_add_f32_e32 v43, v90, v91
	v_pk_mul_f32 v[68:69], v[44:45], v[74:75] op_sel_hi:[1,0]
	v_add_f32_e32 v42, v42, v43
	v_mov_b32_e32 v43, v42
	s_nop 1
	v_permlane32_swap_b32_e32 v42, v43
	v_add_f32_e32 v42, v42, v43
	v_rcp_f32_e32 v42, v42
	v_add_f32_e32 v44, v107, v106
	v_add_f32_e32 v45, v88, v89
	v_pk_mul_f32 v[72:73], v[48:49], v[74:75] op_sel_hi:[1,0]
	v_add_f32_e32 v44, v44, v45
	v_pk_mul_f32 v[36:37], v[36:37], v[74:75] op_sel_hi:[1,0]
	v_pk_mul_f32 v[38:39], v[38:39], v[74:75] op_sel_hi:[1,0]
	v_pk_mul_f32 v[40:41], v[40:41], v[74:75] op_sel_hi:[1,0]
	v_pk_mul_f32 v[34:35], v[34:35], v[74:75] op_sel_hi:[1,0]
	v_pk_mul_f32 v[74:75], v[58:59], v[42:43] op_sel_hi:[1,0]
	v_pk_mul_f32 v[78:79], v[60:61], v[42:43] op_sel_hi:[1,0]
	v_pk_mul_f32 v[80:81], v[62:63], v[42:43] op_sel_hi:[1,0]
	v_pk_mul_f32 v[82:83], v[64:65], v[42:43] op_sel_hi:[1,0]
	v_pk_mul_f32 v[92:93], v[52:53], v[42:43] op_sel_hi:[1,0]
	v_mov_b32_e32 v43, v44
	s_nop 1
	v_permlane32_swap_b32_e32 v44, v43
	v_add_f32_e32 v43, v44, v43
	v_rcp_f32_e32 v76, v43
	v_pk_mul_f32 v[96:97], v[54:55], v[42:43] op_sel_hi:[1,0]
	v_pk_mul_f32 v[94:95], v[56:57], v[42:43] op_sel_hi:[1,0]
	v_pk_mul_f32 v[98:99], v[50:51], v[42:43] op_sel_hi:[1,0]
	v_pk_mul_f32 v[100:101], v[4:5], v[76:77] op_sel_hi:[1,0]
	v_pk_mov_b32 v[4:5], v[86:87], v[84:85] op_sel:[1,0]
	v_mov_b32_e32 v87, v85
	v_pk_add_f32 v[4:5], v[4:5], v[86:87]
	v_pk_mul_f32 v[102:103], v[6:7], v[76:77] op_sel_hi:[1,0]
	v_pk_add_f32 v[104:105], v[4:5], v[4:5] op_sel:[0,1] op_sel_hi:[1,0]
	v_cvt_pk_bf16_f32 v7, v40, v41
	ds_read_b128 v[84:87], v150 offset:52224
	ds_read_b128 v[50:53], v150 offset:35840
	ds_read_b128 v[54:57], v150 offset:36864
	ds_read_b128 v[58:61], v150 offset:37888
	ds_read_b128 v[62:65], v150 offset:38912
	v_cvt_pk_bf16_f32 v6, v38, v39
	v_cvt_pk_bf16_f32 v5, v36, v37
	v_cvt_pk_bf16_f32 v4, v34, v35
	ds_read_b128 v[88:91], v150 offset:53248
	ds_read_b128 v[34:37], v150 offset:39936
	ds_read_b128 v[38:41], v150 offset:40960
	ds_read_b128 v[42:45], v150 offset:41984
	ds_read_b128 v[46:49], v150 offset:43008
	v_cvt_pk_bf16_f32 v95, v94, v95
	v_cvt_pk_bf16_f32 v94, v96, v97
	v_cvt_pk_bf16_f32 v93, v92, v93
	v_cvt_pk_bf16_f32 v92, v98, v99
	s_waitcnt lgkmcnt(5)
	v_mfma_f32_32x32x16_bf16 v[50:65], v[84:87], v[4:7], v[50:65]
	v_mul_f32_e32 v10, v10, v76
	v_mul_f32_e32 v11, v11, v76
	v_mul_f32_e32 v12, v12, v76
	v_mul_f32_e32 v13, v13, v76
	v_mul_f32_e32 v8, v8, v76
	v_mul_f32_e32 v9, v9, v76
	v_mov_b32_e32 v77, v104
	s_nop 1
	v_permlane32_swap_b32_e32 v104, v77
	v_cvt_pk_bf16_f32 v73, v72, v73
	s_waitcnt lgkmcnt(0)
	v_mfma_f32_32x32x16_bf16 v[34:49], v[84:87], v[92:95], v[34:49]
	v_cvt_pk_bf16_f32 v72, v70, v71
	v_cvt_pk_bf16_f32 v70, v66, v67
	v_add_f32_e32 v66, v104, v77
	v_cvt_pk_bf16_f32 v71, v68, v69
	v_rcp_f32_e32 v104, v66
	v_cvt_pk_bf16_f32 v69, v82, v83
	v_cvt_pk_bf16_f32 v68, v80, v81
	v_cvt_pk_bf16_f32 v67, v78, v79
	v_cvt_pk_bf16_f32 v66, v74, v75
	ds_read_b128 v[78:81], v150 offset:54272
	v_mfma_f32_32x32x16_bf16 v[50:65], v[88:91], v[70:73], v[50:65]
	v_mul_f32_e32 v2, v2, v76
	v_mul_f32_e32 v3, v3, v76
	v_mul_f32_e32 v20, v20, v104
	v_mul_f32_e32 v21, v21, v104
	v_cvt_pk_bf16_f32 v85, v8, v9
	v_cvt_pk_bf16_f32 v82, v2, v3
	v_pk_mul_f32 v[2:3], v[22:23], v[104:105] op_sel_hi:[1,0]
	v_pk_mul_f32 v[8:9], v[24:25], v[104:105] op_sel_hi:[1,0]
	v_pk_mul_f32 v[18:19], v[18:19], v[104:105] op_sel_hi:[1,0]
	v_mfma_f32_32x32x16_bf16 v[34:49], v[88:91], v[66:69], v[34:49]
	v_cvt_pk_bf16_f32 v84, v102, v103
	v_cvt_pk_bf16_f32 v83, v100, v101
	ds_read_b128 v[86:89], v150 offset:55296
	v_cvt_pk_bf16_f32 v99, v8, v9
	v_cvt_pk_bf16_f32 v98, v2, v3
	v_cvt_pk_bf16_f32 v97, v20, v21
	v_cvt_pk_bf16_f32 v96, v18, v19
	s_waitcnt lgkmcnt(1)
	v_mfma_f32_32x32x16_bf16 v[50:65], v[78:81], v[82:85], v[50:65]
	v_mul_f32_e32 v2, v14, v76
	v_mul_f32_e32 v3, v15, v76
	v_mul_f32_e32 v8, v16, v76
	v_mul_f32_e32 v9, v17, v76
	v_mul_f32_e32 v14, v26, v104
	v_mul_f32_e32 v15, v27, v104
	v_cvt_pk_bf16_f32 v77, v8, v9
	v_cvt_pk_bf16_f32 v76, v2, v3
	v_cvt_pk_bf16_f32 v74, v10, v11
	v_pk_mul_f32 v[2:3], v[28:29], v[104:105] op_sel_hi:[1,0]
	v_mfma_f32_32x32x16_bf16 v[34:49], v[78:81], v[96:99], v[34:49]
	v_mul_f32_e32 v8, v30, v104
	v_mul_f32_e32 v9, v31, v104
	v_mul_f32_e32 v10, v32, v104
	v_mul_f32_e32 v11, v33, v104
	v_cvt_pk_bf16_f32 v75, v12, v13
	v_cvt_pk_bf16_f32 v81, v10, v11
	v_cvt_pk_bf16_f32 v80, v8, v9
	v_cvt_pk_bf16_f32 v79, v2, v3
	v_cvt_pk_bf16_f32 v78, v14, v15
	s_waitcnt lgkmcnt(0)
	v_mfma_f32_32x32x16_bf16 v[50:65], v[86:89], v[74:77], v[50:65]
	v_mfma_f32_32x32x16_bf16 v[34:49], v[86:89], v[78:81], v[34:49]
	ds_read_b128 v[86:89], v150 offset:56320
	ds_read_b128 v[18:21], v150 offset:44032
	ds_read_b128 v[22:25], v150 offset:45056
	ds_read_b128 v[26:29], v150 offset:46080
	ds_read_b128 v[30:33], v150 offset:47104
	ds_read_b128 v[100:103], v150 offset:57344
	s_waitcnt lgkmcnt(1)
	v_mfma_f32_32x32x16_bf16 v[18:33], v[86:89], v[4:7], v[18:33]
	ds_read_b128 v[2:5], v150 offset:48128
	ds_read_b128 v[6:9], v150 offset:49152
	ds_read_b128 v[10:13], v150 offset:50176
	ds_read_b128 v[14:17], v150 offset:51200
	s_waitcnt lgkmcnt(0)
	v_mfma_f32_32x32x16_bf16 v[2:17], v[86:89], v[92:95], v[2:17]
	v_mfma_f32_32x32x16_bf16 v[18:33], v[100:103], v[70:73], v[18:33]
	v_mfma_f32_32x32x16_bf16 v[2:17], v[100:103], v[66:69], v[2:17]
	ds_read_b128 v[66:69], v150 offset:58368
	ds_read_b128 v[70:73], v150 offset:59392
	s_waitcnt lgkmcnt(1)
	v_mfma_f32_32x32x16_bf16 v[18:33], v[66:69], v[82:85], v[18:33]
	v_mfma_f32_32x32x16_bf16 v[2:17], v[66:69], v[96:99], v[2:17]
	s_waitcnt lgkmcnt(0)
	v_mfma_f32_32x32x16_bf16 v[18:33], v[70:73], v[74:77], v[18:33]
	v_mfma_f32_32x32x16_bf16 v[2:17], v[70:73], v[78:81], v[2:17]
	s_nop 10
	v_mul_f32_e32 v66, v22, v22
	v_mul_f32_e32 v67, v23, v23
	v_mul_f32_e32 v68, v30, v30
	v_mul_f32_e32 v69, v31, v31
	v_mul_f32_e32 v70, v24, v24
	v_mul_f32_e32 v71, v25, v25
	v_pk_mul_f32 v[72:73], v[32:33], v[32:33]
	v_pk_mul_f32 v[74:75], v[20:21], v[20:21]
	v_pk_mul_f32 v[76:77], v[28:29], v[28:29]
	v_pk_mul_f32 v[78:79], v[26:27], v[26:27]
	v_pk_mul_f32 v[80:81], v[18:19], v[18:19]
	v_pk_fma_f32 v[78:79], v[58:59], v[58:59], v[78:79]
	v_pk_fma_f32 v[76:77], v[60:61], v[60:61], v[76:77]
	v_pk_fma_f32 v[74:75], v[52:53], v[52:53], v[74:75]
	v_pk_fma_f32 v[72:73], v[64:65], v[64:65], v[72:73]
	v_pk_fma_f32 v[70:71], v[56:57], v[56:57], v[70:71]
	v_pk_fma_f32 v[68:69], v[62:63], v[62:63], v[68:69]
	v_pk_fma_f32 v[66:67], v[54:55], v[54:55], v[66:67]
	v_pk_fma_f32 v[80:81], v[50:51], v[50:51], v[80:81]
	v_pk_add_f32 v[66:67], v[66:67], v[68:69]
	v_pk_add_f32 v[68:69], v[70:71], v[72:73]
	v_pk_add_f32 v[70:71], v[74:75], v[76:77]
	v_pk_add_f32 v[72:73], v[80:81], v[78:79]
	v_pk_add_f32 v[68:69], v[70:71], v[68:69]
	v_pk_add_f32 v[66:67], v[72:73], v[66:67]
	v_pk_mul_f32 v[72:73], v[14:15], v[14:15]
	v_pk_mov_b32 v[70:71], v[66:67], v[68:69] op_sel:[1,0]
	v_mov_b32_e32 v67, v69
	v_pk_add_f32 v[66:67], v[70:71], v[66:67]
	v_pk_mul_f32 v[70:71], v[6:7], v[6:7]
	v_pk_mul_f32 v[74:75], v[8:9], v[8:9]
	v_pk_mul_f32 v[76:77], v[16:17], v[16:17]
	v_pk_mul_f32 v[78:79], v[4:5], v[4:5]
	v_pk_mul_f32 v[80:81], v[12:13], v[12:13]
	v_pk_mul_f32 v[82:83], v[10:11], v[10:11]
	v_pk_mul_f32 v[84:85], v[2:3], v[2:3]
	v_pk_fma_f32 v[82:83], v[42:43], v[42:43], v[82:83]
	v_pk_fma_f32 v[80:81], v[44:45], v[44:45], v[80:81]
	v_pk_fma_f32 v[78:79], v[36:37], v[36:37], v[78:79]
	v_pk_fma_f32 v[76:77], v[48:49], v[48:49], v[76:77]
	v_pk_fma_f32 v[74:75], v[40:41], v[40:41], v[74:75]
	v_pk_fma_f32 v[72:73], v[46:47], v[46:47], v[72:73]
	v_pk_fma_f32 v[70:71], v[38:39], v[38:39], v[70:71]
	v_pk_fma_f32 v[84:85], v[34:35], v[34:35], v[84:85]
	v_pk_add_f32 v[70:71], v[70:71], v[72:73]
	v_pk_add_f32 v[72:73], v[74:75], v[76:77]
	v_pk_add_f32 v[74:75], v[78:79], v[80:81]
	v_pk_add_f32 v[76:77], v[84:85], v[82:83]
	v_pk_add_f32 v[72:73], v[74:75], v[72:73]
	v_pk_add_f32 v[70:71], v[76:77], v[70:71]
	v_pk_add_f32 v[66:67], v[66:67], v[66:67] op_sel:[0,1] op_sel_hi:[1,0]
	v_add_f32_e32 v70, v71, v70
	v_add_f32_e32 v71, v72, v73
	v_mov_b32_e32 v69, v66
	v_add_f32_e32 v70, v70, v71
	s_nop 0
	v_permlane32_swap_b32_e32 v66, v69
	v_mov_b32_e32 v68, v70
	s_nop 1
	v_permlane32_swap_b32_e32 v70, v68
	v_mov_b32_e32 v71, v66
	v_pk_add_f32 v[66:67], v[70:71], v[68:69]
	v_pk_fma_f32 v[66:67], v[66:67], s[0:1], v[152:153] op_sel_hi:[1,0,0]
	s_mov_b32 s1, 0x800000
	v_rsq_f32_e32 v68, v67
	s_nop 0
	v_pk_mul_f32 v[158:159], v[50:51], v[68:69] op_sel_hi:[1,0]
	v_pk_mul_f32 v[50:51], v[18:19], v[68:69] op_sel_hi:[1,0]
	v_pk_mul_f32 v[80:81], v[60:61], v[68:69] op_sel_hi:[1,0]
	v_pk_mul_f32 v[60:61], v[28:29], v[68:69] op_sel_hi:[1,0]
	v_pk_mul_f32 v[78:79], v[58:59], v[68:69] op_sel_hi:[1,0]
	v_pk_mul_f32 v[160:161], v[52:53], v[68:69] op_sel_hi:[1,0]
	v_pk_mul_f32 v[82:83], v[54:55], v[68:69] op_sel_hi:[1,0]
	v_rsq_f32_e32 v28, v66
	v_pk_mul_f32 v[168:169], v[56:57], v[68:69] op_sel_hi:[1,0]
	v_pk_mul_f32 v[58:59], v[26:27], v[68:69] op_sel_hi:[1,0]
	v_pk_mul_f32 v[52:53], v[20:21], v[68:69] op_sel_hi:[1,0]
	v_pk_mul_f32 v[54:55], v[22:23], v[68:69] op_sel_hi:[1,0]
	v_pk_mul_f32 v[56:57], v[24:25], v[68:69] op_sel_hi:[1,0]
	v_pk_mul_f32 v[18:19], v[42:43], v[28:29] op_sel_hi:[1,0]
	v_pk_mul_f32 v[20:21], v[44:45], v[28:29] op_sel_hi:[1,0]
	v_pk_mul_f32 v[22:23], v[46:47], v[28:29] op_sel_hi:[1,0]
	v_pk_mul_f32 v[26:27], v[48:49], v[28:29] op_sel_hi:[1,0]
	v_pk_mul_f32 v[162:163], v[34:35], v[28:29] op_sel_hi:[1,0]
	v_pk_mul_f32 v[164:165], v[36:37], v[28:29] op_sel_hi:[1,0]
	v_pk_mul_f32 v[166:167], v[38:39], v[28:29] op_sel_hi:[1,0]
	v_pk_mul_f32 v[24:25], v[40:41], v[28:29] op_sel_hi:[1,0]
	v_pk_mul_f32 v[104:105], v[2:3], v[28:29] op_sel_hi:[1,0]
	v_pk_mul_f32 v[112:113], v[4:5], v[28:29] op_sel_hi:[1,0]
	ds_read_b128 v[2:5], v150 offset:60416
	ds_read_b128 v[34:37], v174 offset:32768
	ds_read_b128 v[38:41], v174 offset:32800
	ds_read_b128 v[42:45], v174 offset:32832
	ds_read_b128 v[46:49], v174 offset:32864
	v_cvt_pk_bf16_f32 v129, v168, v169
	v_cvt_pk_bf16_f32 v128, v82, v83
	v_cvt_pk_bf16_f32 v127, v160, v161
	v_cvt_pk_bf16_f32 v126, v158, v159
	v_cvt_pk_bf16_f32 v137, v24, v25
	v_cvt_pk_bf16_f32 v136, v166, v167
	v_cvt_pk_bf16_f32 v135, v164, v165
	s_waitcnt lgkmcnt(0)
	v_mfma_f32_32x32x16_bf16 v[86:101], v[2:5], v[126:129], v[34:49]
	v_cvt_pk_bf16_f32 v134, v162, v163
	v_mul_f32_e32 v84, v62, v68
	v_mul_f32_e32 v85, v63, v68
	v_mul_f32_e32 v170, v64, v68
	v_mul_f32_e32 v171, v65, v68
	v_pk_mul_f32 v[62:63], v[30:31], v[68:69] op_sel_hi:[1,0]
	v_pk_mul_f32 v[64:65], v[32:33], v[68:69] op_sel_hi:[1,0]
	v_pk_mul_f32 v[116:117], v[6:7], v[28:29] op_sel_hi:[1,0]
	v_pk_mul_f32 v[154:155], v[8:9], v[28:29] op_sel_hi:[1,0]
	v_mfma_f32_32x32x16_bf16 v[34:49], v[2:5], v[134:137], v[34:49]
	ds_read_b128 v[6:9], v150 offset:61440
	ds_read_b128 v[66:69], v174 offset:32896
	ds_read_b128 v[106:109], v150 offset:64512
	v_cvt_pk_bf16_f32 v125, v170, v171
	v_cvt_pk_bf16_f32 v124, v84, v85
	v_cvt_pk_bf16_f32 v123, v80, v81
	v_cvt_pk_bf16_f32 v122, v78, v79
	v_cvt_pk_bf16_f32 v149, v26, v27
	v_cvt_pk_bf16_f32 v148, v22, v23
	v_cvt_pk_bf16_f32 v147, v20, v21
	v_cvt_pk_bf16_f32 v146, v18, v19
	s_waitcnt lgkmcnt(2)
	v_mfma_f32_32x32x16_bf16 v[86:101], v[6:9], v[122:125], v[86:101]
	v_mul_f32_e32 v102, v10, v28
	v_mul_f32_e32 v103, v11, v28
	v_mul_f32_e32 v110, v12, v28
	v_mul_f32_e32 v111, v13, v28
	v_mul_f32_e32 v114, v14, v28
	v_mul_f32_e32 v115, v15, v28
	v_pk_mul_f32 v[156:157], v[16:17], v[28:29] op_sel_hi:[1,0]
	ds_read_b128 v[176:179], v174 offset:33536
	ds_read_b128 v[180:183], v174 offset:33568
	ds_read_b128 v[184:187], v174 offset:33600
	ds_read_b128 v[28:31], v174 offset:33632
	ds_read_b128 v[188:191], v174 offset:33792
	ds_read_b128 v[192:195], v174 offset:33824
	ds_read_b128 v[196:199], v174 offset:33856
	ds_read_b128 v[200:203], v174 offset:33888
	ds_read_b128 v[204:207], v150 offset:62464
	v_cvt_pk_bf16_f32 v133, v56, v57
	v_mfma_f32_32x32x16_bf16 v[34:49], v[6:9], v[146:149], v[34:49]
	v_cvt_pk_bf16_f32 v132, v54, v55
	v_cvt_pk_bf16_f32 v131, v52, v53
	v_cvt_pk_bf16_f32 v130, v50, v51
	ds_read_b128 v[70:73], v174 offset:33664
	ds_read_b128 v[74:77], v174 offset:33920
	ds_read_b128 v[208:211], v150 offset:63488
	v_cvt_pk_bf16_f32 v145, v154, v155
	v_cvt_pk_bf16_f32 v144, v116, v117
	v_cvt_pk_bf16_f32 v143, v112, v113
	v_cvt_pk_bf16_f32 v142, v104, v105
	s_waitcnt lgkmcnt(3)
	v_mfma_f32_32x32x16_bf16 v[86:101], v[204:207], v[130:133], v[86:101]
	v_cvt_pk_bf16_f32 v121, v64, v65
	v_cvt_pk_bf16_f32 v120, v62, v63
	v_cvt_pk_bf16_f32 v119, v60, v61
	v_cvt_pk_bf16_f32 v118, v58, v59
	v_cvt_pk_bf16_f32 v141, v156, v157
	v_cvt_pk_bf16_f32 v140, v114, v115
	v_cvt_pk_bf16_f32 v139, v110, v111
	v_mfma_f32_32x32x16_bf16 v[34:49], v[204:207], v[142:145], v[34:49]
	v_cvt_pk_bf16_f32 v138, v102, v103
	v_fma_f32 v16, v30, v170, v202
	v_fma_f32 v17, v31, v171, v203
	v_fma_f32 v14, v28, v84, v200
	v_fma_f32 v15, v29, v85, v201
	v_pk_fma_f32 v[12:13], v[186:187], v[80:81], v[198:199]
	v_pk_fma_f32 v[10:11], v[184:185], v[78:79], v[196:197]
	v_pk_fma_f32 v[8:9], v[182:183], v[168:169], v[194:195]
	s_waitcnt lgkmcnt(0)
	v_mfma_f32_32x32x16_bf16 v[86:101], v[208:211], v[118:121], v[86:101]
	v_fma_f32 v6, v180, v82, v192
	v_fma_f32 v7, v181, v83, v193
	ds_read_b128 v[78:81], v174 offset:33760
	ds_read_b128 v[82:85], v174 offset:33248
	v_fma_f32 v4, v178, v160, v190
	v_fma_f32 v5, v179, v161, v191
	v_pk_fma_f32 v[2:3], v[176:177], v[158:159], v[188:189]
	v_pk_fma_f32 v[32:33], v[30:31], v[26:27], v[202:203]
	v_pk_fma_f32 v[30:31], v[28:29], v[22:23], v[200:201]
	v_pk_fma_f32 v[28:29], v[186:187], v[20:21], v[198:199]
	v_pk_fma_f32 v[26:27], v[184:185], v[18:19], v[196:197]
	v_pk_fma_f32 v[24:25], v[182:183], v[24:25], v[194:195]
	v_pk_fma_f32 v[22:23], v[180:181], v[166:167], v[192:193]
	v_pk_fma_f32 v[20:21], v[178:179], v[164:165], v[190:191]
	v_pk_fma_f32 v[18:19], v[176:177], v[162:163], v[188:189]
	ds_read_b128 v[158:161], v174 offset:33696
	ds_read_b128 v[162:165], v174 offset:33728
	ds_read_b128 v[166:169], v174 offset:33952
	ds_read_b128 v[176:179], v174 offset:33984
	ds_read_b128 v[180:183], v174 offset:34016
	ds_read_b128 v[184:187], v212 offset:11264
	v_mfma_f32_32x32x16_bf16 v[34:49], v[208:211], v[138:141], v[34:49]
	v_cvt_pk_bf16_f32 v86, v86, v87
	v_cvt_pk_bf16_f32 v87, v88, v89
	v_cvt_pk_bf16_f32 v88, v90, v91
	v_cvt_pk_bf16_f32 v89, v92, v93
	ds_read_b128 v[90:93], v212 offset:12288
	v_pk_max_i16 v86, v86, 0
	v_pk_max_i16 v87, v87, 0
	v_pk_max_i16 v88, v88, 0
	v_pk_max_i16 v89, v89, 0
	s_nop 1
	s_nop 0
	v_cvt_pk_bf16_f32 v188, v34, v35
	v_cvt_pk_bf16_f32 v189, v36, v37
	v_cvt_pk_bf16_f32 v190, v38, v39
	v_cvt_pk_bf16_f32 v191, v40, v41
	s_waitcnt lgkmcnt(1)
	v_mfma_f32_32x32x16_bf16 v[2:17], v[184:187], v[86:89], v[2:17]
	v_pk_max_i16 v188, v188, 0
	v_pk_max_i16 v189, v189, 0
	v_pk_max_i16 v190, v190, 0
	v_pk_max_i16 v191, v191, 0
	v_cvt_pk_bf16_f32 v94, v94, v95
	v_cvt_pk_bf16_f32 v95, v96, v97
	v_cvt_pk_bf16_f32 v96, v98, v99
	v_cvt_pk_bf16_f32 v97, v100, v101
	v_cvt_pk_bf16_f32 v98, v42, v43
	v_cvt_pk_bf16_f32 v99, v44, v45
	v_mfma_f32_32x32x16_bf16 v[18:33], v[184:187], v[188:191], v[18:33]
	ds_read_b128 v[184:187], v212 offset:19456
	v_cvt_pk_bf16_f32 v100, v46, v47
	v_cvt_pk_bf16_f32 v101, v48, v49
	v_fma_f32 v64, v80, v64, v182
	v_fma_f32 v65, v81, v65, v183
	v_pk_fma_f32 v[62:63], v[78:79], v[62:63], v[180:181]
	v_pk_fma_f32 v[60:61], v[164:165], v[60:61], v[178:179]
	v_pk_fma_f32 v[58:59], v[162:163], v[58:59], v[176:177]
	v_pk_max_i16 v94, v94, 0
	v_pk_max_i16 v95, v95, 0
	v_pk_max_i16 v96, v96, 0
	v_pk_max_i16 v97, v97, 0
	v_pk_max_i16 v98, v98, 0
	v_pk_max_i16 v99, v99, 0
	v_pk_max_i16 v100, v100, 0
	v_pk_max_i16 v101, v101, 0
	v_pk_fma_f32 v[56:57], v[160:161], v[56:57], v[168:169]
	s_waitcnt lgkmcnt(1)
	v_mfma_f32_32x32x16_bf16 v[2:17], v[90:93], v[94:97], v[2:17]
	v_fma_f32 v54, v158, v54, v166
	v_fma_f32 v55, v159, v55, v167
	v_fma_f32 v52, v72, v52, v76
	v_fma_f32 v53, v73, v53, v77
	v_fma_f32 v50, v70, v50, v74
	v_fma_f32 v51, v71, v51, v75
	v_pk_fma_f32 v[48:49], v[80:81], v[156:157], v[182:183]
	v_pk_fma_f32 v[46:47], v[78:79], v[114:115], v[180:181]
	v_pk_fma_f32 v[44:45], v[164:165], v[110:111], v[178:179]
	v_pk_fma_f32 v[42:43], v[162:163], v[102:103], v[176:177]
	v_mfma_f32_32x32x16_bf16 v[18:33], v[90:93], v[98:101], v[18:33]
	ds_read_b128 v[90:93], v212 offset:20480
	v_fma_f32 v40, v160, v154, v168
	v_fma_f32 v41, v161, v155, v169
	v_fma_f32 v38, v158, v116, v166
	v_fma_f32 v39, v159, v117, v167
	v_pk_fma_f32 v[36:37], v[72:73], v[112:113], v[76:77]
	v_pk_fma_f32 v[34:35], v[70:71], v[104:105], v[74:75]
	s_waitcnt lgkmcnt(1)
	v_mfma_f32_32x32x16_bf16 v[50:65], v[184:187], v[86:89], v[50:65]
	ds_read_b128 v[70:73], v174 offset:32928
	ds_read_b128 v[74:77], v174 offset:32960
	ds_read_b128 v[78:81], v174 offset:32992
	ds_read_b128 v[86:89], v174 offset:33024
	ds_read_b128 v[110:113], v212 offset:1024
	v_mfma_f32_32x32x16_bf16 v[34:49], v[184:187], v[188:191], v[34:49]
	s_waitcnt lgkmcnt(5)
	v_mfma_f32_32x32x16_bf16 v[50:65], v[90:93], v[94:97], v[50:65]
	v_mfma_f32_32x32x16_bf16 v[34:49], v[90:93], v[98:101], v[34:49]
	s_waitcnt lgkmcnt(2)
	v_mfma_f32_32x32x16_bf16 v[90:105], v[106:109], v[126:129], v[66:81]
	v_mfma_f32_32x32x16_bf16 v[66:81], v[106:109], v[134:137], v[66:81]
	ds_read_b128 v[106:109], v212 offset:0
	s_waitcnt lgkmcnt(0)
	v_mfma_f32_32x32x16_bf16 v[90:105], v[106:109], v[122:125], v[90:105]
	v_mfma_f32_32x32x16_bf16 v[66:81], v[106:109], v[146:149], v[66:81]
	ds_read_b128 v[106:109], v212 offset:2048
	v_mfma_f32_32x32x16_bf16 v[90:105], v[110:113], v[130:133], v[90:105]
	v_mfma_f32_32x32x16_bf16 v[66:81], v[110:113], v[142:145], v[66:81]
	ds_read_b128 v[110:113], v212 offset:13312
	s_waitcnt lgkmcnt(1)
	v_mfma_f32_32x32x16_bf16 v[90:105], v[106:109], v[118:121], v[90:105]
	v_mfma_f32_32x32x16_bf16 v[66:81], v[106:109], v[138:141], v[66:81]
	s_nop 10
	v_cvt_pk_bf16_f32 v90, v90, v91
	v_cvt_pk_bf16_f32 v91, v92, v93
	v_cvt_pk_bf16_f32 v92, v94, v95
	v_cvt_pk_bf16_f32 v94, v98, v99
	v_cvt_pk_bf16_f32 v95, v100, v101
	ds_read_b128 v[98:101], v212 offset:21504
	v_cvt_pk_bf16_f32 v66, v66, v67
	v_cvt_pk_bf16_f32 v67, v68, v69
	v_cvt_pk_bf16_f32 v68, v70, v71
	v_cvt_pk_bf16_f32 v93, v96, v97
	v_cvt_pk_bf16_f32 v69, v72, v73
	ds_read_b128 v[70:73], v212 offset:14336
	v_pk_max_i16 v90, v90, 0
	v_pk_max_i16 v91, v91, 0
	v_pk_max_i16 v92, v92, 0
	v_pk_max_i16 v93, v93, 0
	v_pk_max_i16 v66, v66, 0
	v_pk_max_i16 v67, v67, 0
	v_pk_max_i16 v68, v68, 0
	v_pk_max_i16 v69, v69, 0
	v_cvt_pk_bf16_f32 v96, v102, v103
	s_waitcnt lgkmcnt(2)
	v_mfma_f32_32x32x16_bf16 v[2:17], v[110:113], v[90:93], v[2:17]
	v_cvt_pk_bf16_f32 v97, v104, v105
	v_cvt_pk_bf16_f32 v74, v74, v75
	v_cvt_pk_bf16_f32 v75, v76, v77
	v_cvt_pk_bf16_f32 v76, v78, v79
	v_cvt_pk_bf16_f32 v77, v80, v81
	v_pk_max_i16 v94, v94, 0
	v_pk_max_i16 v95, v95, 0
	v_pk_max_i16 v96, v96, 0
	v_pk_max_i16 v97, v97, 0
	v_pk_max_i16 v74, v74, 0
	v_pk_max_i16 v75, v75, 0
	v_pk_max_i16 v76, v76, 0
	v_pk_max_i16 v77, v77, 0
	v_mfma_f32_32x32x16_bf16 v[18:33], v[110:113], v[66:69], v[18:33]
	s_waitcnt lgkmcnt(1)
	v_mfma_f32_32x32x16_bf16 v[34:49], v[98:101], v[66:69], v[34:49]
	ds_read_b128 v[66:69], v212 offset:22528
	v_mfma_f32_32x32x16_bf16 v[50:65], v[98:101], v[90:93], v[50:65]
	s_waitcnt lgkmcnt(1)
	v_mfma_f32_32x32x16_bf16 v[2:17], v[70:73], v[94:97], v[2:17]
	v_mfma_f32_32x32x16_bf16 v[18:33], v[70:73], v[74:77], v[18:33]
	ds_read_b128 v[78:81], v212 offset:3072
	s_waitcnt lgkmcnt(1)
	v_mfma_f32_32x32x16_bf16 v[50:65], v[66:69], v[94:97], v[50:65]
	ds_read_b128 v[90:93], v174 offset:33056
	ds_read_b128 v[94:97], v174 offset:33088
	ds_read_b128 v[98:101], v174 offset:33120
	ds_read_b128 v[70:73], v174 offset:33152
	v_mfma_f32_32x32x16_bf16 v[34:49], v[66:69], v[74:77], v[34:49]
	ds_read_b128 v[66:69], v212 offset:4096
	ds_read_b128 v[74:77], v212 offset:5120
	s_waitcnt lgkmcnt(3)
	v_mfma_f32_32x32x16_bf16 v[102:117], v[78:81], v[126:129], v[86:101]
	v_mfma_f32_32x32x16_bf16 v[86:101], v[78:81], v[134:137], v[86:101]
	s_waitcnt lgkmcnt(1)
	v_mfma_f32_32x32x16_bf16 v[86:101], v[66:69], v[146:149], v[86:101]
	v_mfma_f32_32x32x16_bf16 v[102:117], v[66:69], v[122:125], v[102:117]
	ds_read_b128 v[66:69], v212 offset:6144
	s_waitcnt lgkmcnt(1)
	v_mfma_f32_32x32x16_bf16 v[86:101], v[74:77], v[142:145], v[86:101]
	v_mfma_f32_32x32x16_bf16 v[102:117], v[74:77], v[130:133], v[102:117]
	ds_read_b128 v[74:77], v212 offset:15360
	s_waitcnt lgkmcnt(1)
	v_mfma_f32_32x32x16_bf16 v[86:101], v[66:69], v[138:141], v[86:101]
	v_mfma_f32_32x32x16_bf16 v[102:117], v[66:69], v[118:121], v[102:117]
	s_nop 10
	v_cvt_pk_bf16_f32 v78, v86, v87
	v_cvt_pk_bf16_f32 v80, v90, v91
	v_cvt_pk_bf16_f32 v79, v88, v89
	v_cvt_pk_bf16_f32 v81, v92, v93
	ds_read_b128 v[86:89], v212 offset:16384
	ds_read_b128 v[90:93], v212 offset:23552
	v_cvt_pk_bf16_f32 v66, v102, v103
	v_cvt_pk_bf16_f32 v67, v104, v105
	v_cvt_pk_bf16_f32 v68, v106, v107
	v_cvt_pk_bf16_f32 v69, v108, v109
	v_pk_max_i16 v66, v66, 0
	v_pk_max_i16 v67, v67, 0
	v_pk_max_i16 v68, v68, 0
	v_pk_max_i16 v69, v69, 0
	v_pk_max_i16 v78, v78, 0
	v_pk_max_i16 v79, v79, 0
	v_pk_max_i16 v80, v80, 0
	v_pk_max_i16 v81, v81, 0
	v_cvt_pk_bf16_f32 v94, v94, v95
	s_waitcnt lgkmcnt(2)
	v_mfma_f32_32x32x16_bf16 v[18:33], v[74:77], v[78:81], v[18:33]
	v_cvt_pk_bf16_f32 v95, v96, v97
	v_cvt_pk_bf16_f32 v96, v98, v99
	v_cvt_pk_bf16_f32 v97, v100, v101
	v_pk_max_i16 v94, v94, 0
	v_pk_max_i16 v95, v95, 0
	v_pk_max_i16 v96, v96, 0
	v_pk_max_i16 v97, v97, 0
	v_mfma_f32_32x32x16_bf16 v[2:17], v[74:77], v[66:69], v[2:17]
	v_cvt_pk_bf16_f32 v74, v110, v111
	v_cvt_pk_bf16_f32 v75, v112, v113
	v_cvt_pk_bf16_f32 v76, v114, v115
	v_cvt_pk_bf16_f32 v77, v116, v117
	v_pk_max_i16 v74, v74, 0
	v_pk_max_i16 v75, v75, 0
	v_pk_max_i16 v76, v76, 0
	v_pk_max_i16 v77, v77, 0
	s_waitcnt lgkmcnt(0)
	v_mfma_f32_32x32x16_bf16 v[50:65], v[90:93], v[66:69], v[50:65]
	ds_read_b128 v[66:69], v212 offset:24576
	v_mfma_f32_32x32x16_bf16 v[34:49], v[90:93], v[78:81], v[34:49]
	ds_read_b128 v[102:105], v212 offset:7168
	v_mfma_f32_32x32x16_bf16 v[2:17], v[86:89], v[74:77], v[2:17]
	s_waitcnt lgkmcnt(1)
	v_mfma_f32_32x32x16_bf16 v[50:65], v[66:69], v[74:77], v[50:65]
	ds_read_b128 v[74:77], v174 offset:33184
	ds_read_b128 v[78:81], v174 offset:33216
	v_mfma_f32_32x32x16_bf16 v[34:49], v[66:69], v[94:97], v[34:49]
	ds_read_b128 v[66:69], v212 offset:8192
	v_mfma_f32_32x32x16_bf16 v[18:33], v[86:89], v[94:97], v[18:33]
	s_waitcnt lgkmcnt(1)
	v_mfma_f32_32x32x16_bf16 v[86:101], v[102:105], v[126:129], v[70:85]
	v_mfma_f32_32x32x16_bf16 v[70:85], v[102:105], v[134:137], v[70:85]
	ds_read_b128 v[102:105], v212 offset:9216
	v_lshlrev_b32_e32 v135, 2, v1
	v_add_u32_e32 v134, v172, v174
	s_waitcnt lgkmcnt(1)
	v_mfma_f32_32x32x16_bf16 v[86:101], v[66:69], v[122:125], v[86:101]
	v_mfma_f32_32x32x16_bf16 v[70:85], v[66:69], v[146:149], v[70:85]
	ds_read_b128 v[66:69], v212 offset:10240
	s_waitcnt lgkmcnt(1)
	v_mfma_f32_32x32x16_bf16 v[86:101], v[102:105], v[130:133], v[86:101]
	v_mfma_f32_32x32x16_bf16 v[70:85], v[102:105], v[142:145], v[70:85]
	ds_read_b128 v[102:105], v212 offset:17408
	s_waitcnt lgkmcnt(1)
	v_mfma_f32_32x32x16_bf16 v[86:101], v[66:69], v[118:121], v[86:101]
	v_mfma_f32_32x32x16_bf16 v[70:85], v[66:69], v[138:141], v[70:85]
	s_nop 10
	v_cvt_pk_bf16_f32 v68, v90, v91
	v_cvt_pk_bf16_f32 v69, v92, v93
	ds_read_b128 v[90:93], v212 offset:25600
	v_cvt_pk_bf16_f32 v66, v86, v87
	v_cvt_pk_bf16_f32 v67, v88, v89
	v_pk_max_i16 v66, v66, 0
	v_pk_max_i16 v67, v67, 0
	v_pk_max_i16 v68, v68, 0
	v_pk_max_i16 v69, v69, 0
	v_cvt_pk_bf16_f32 v70, v70, v71
	v_cvt_pk_bf16_f32 v71, v72, v73
	s_waitcnt lgkmcnt(1)
	v_mfma_f32_32x32x16_bf16 v[2:17], v[102:105], v[66:69], v[2:17]
	v_cvt_pk_bf16_f32 v72, v74, v75
	v_cvt_pk_bf16_f32 v73, v76, v77
	ds_read_b128 v[74:77], v212 offset:18432
	v_cvt_pk_bf16_f32 v86, v94, v95
	v_cvt_pk_bf16_f32 v87, v96, v97
	v_cvt_pk_bf16_f32 v88, v98, v99
	s_waitcnt lgkmcnt(1)
	v_mfma_f32_32x32x16_bf16 v[50:65], v[90:93], v[66:69], v[50:65]
	ds_read_b128 v[66:69], v212 offset:26624
	v_cvt_pk_bf16_f32 v89, v100, v101
	v_pk_max_i16 v86, v86, 0
	v_pk_max_i16 v87, v87, 0
	v_pk_max_i16 v88, v88, 0
	v_pk_max_i16 v89, v89, 0
	v_pk_max_i16 v70, v70, 0
	v_pk_max_i16 v71, v71, 0
	v_pk_max_i16 v72, v72, 0
	v_pk_max_i16 v73, v73, 0
	v_cvt_pk_bf16_f32 v78, v78, v79
	v_cvt_pk_bf16_f32 v79, v80, v81
	s_waitcnt lgkmcnt(1)
	v_mfma_f32_32x32x16_bf16 v[2:17], v[74:77], v[86:89], v[2:17]
	v_cvt_pk_bf16_f32 v80, v82, v83
	v_cvt_pk_bf16_f32 v81, v84, v85
	v_pk_max_i16 v78, v78, 0
	v_pk_max_i16 v79, v79, 0
	v_pk_max_i16 v80, v80, 0
	v_pk_max_i16 v81, v81, 0
	s_waitcnt lgkmcnt(0)
	v_mfma_f32_32x32x16_bf16 v[50:65], v[66:69], v[86:89], v[50:65]
	v_mfma_f32_32x32x16_bf16 v[34:49], v[90:93], v[70:73], v[34:49]
	s_nop 10
	v_add_f32_e32 v130, v10, v58
	v_add_f32_e32 v131, v11, v59
	v_add_f32_e32 v132, v12, v60
	v_add_f32_e32 v133, v13, v61
	v_add_f32_e32 v138, v4, v52
	v_add_f32_e32 v139, v5, v53
	v_pk_add_f32 v[140:141], v[16:17], v[64:65]
	v_pk_add_f32 v[142:143], v[8:9], v[56:57]
	v_pk_add_f32 v[144:145], v[14:15], v[62:63]
	v_pk_add_f32 v[146:147], v[6:7], v[54:55]
	v_mfma_f32_32x32x16_bf16 v[18:33], v[102:105], v[70:73], v[18:33]
	ds_read2st64_b32 v[70:71], v135 offset0:133 offset1:134
	v_add_f32_e32 v148, v2, v50
	v_add_f32_e32 v149, v3, v51
	v_add_f32_e32 v144, v146, v144
	v_add_f32_e32 v145, v147, v145
	v_pk_add_f32 v[140:141], v[142:143], v[140:141]
	v_pk_add_f32 v[132:133], v[138:139], v[132:133]
	v_pk_add_f32 v[130:131], v[148:149], v[130:131]
	v_pk_add_f32 v[132:133], v[132:133], v[140:141]
	v_pk_add_f32 v[130:131], v[130:131], v[144:145]
	v_mfma_f32_32x32x16_bf16 v[34:49], v[66:69], v[78:81], v[34:49]
	s_waitcnt vmcnt(0) lgkmcnt(0)
	v_mul_f32_e32 v66, v175, v70
	v_add_f32_e32 v130, v131, v130
	v_add_f32_e32 v131, v132, v133
	ds_write_b32 v173, v66 offset:512
	v_mul_f32_e32 v66, v175, v71
	v_add_f32_e32 v130, v130, v131
	s_waitcnt lgkmcnt(0)
	ds_read_b128 v[102:105], v174 offset:34560
	ds_read_b128 v[98:101], v174 offset:34592
	ds_read_b128 v[110:113], v174 offset:34624
	ds_read_b128 v[106:109], v174 offset:34656
	ds_read_b128 v[114:117], v174 offset:34688
	ds_read_b128 v[122:125], v174 offset:34720
	ds_read_b128 v[118:121], v174 offset:34752
	ds_read_b128 v[126:129], v174 offset:34784
	v_mov_b32_dpp v66, v66 quad_perm:[1,0,3,2] row_mask:0xf bank_mask:0xf bound_ctrl:1
	v_mov_b32_e32 v131, v130
	v_fmac_f32_e32 v66, v175, v71
	s_nop 0
	v_permlane32_swap_b32_e32 v130, v131
	v_add_f32_dpp v66, v66, v66 quad_perm:[2,3,0,1] row_mask:0xf bank_mask:0xf bound_ctrl:1
	v_add_f32_e32 v130, v130, v131
	v_fmamk_f32 v65, v130, 0xbc800000, v65
	v_add_f32_dpp v66, v66, v66 row_half_mirror row_mask:0xf bank_mask:0xf bound_ctrl:1
	v_fmamk_f32 v64, v130, 0xbc800000, v64
	v_fmamk_f32 v63, v130, 0xbc800000, v63
	v_fmamk_f32 v62, v130, 0xbc800000, v62
	v_fmamk_f32 v61, v130, 0xbc800000, v61
	v_fmamk_f32 v60, v130, 0xbc800000, v60
	v_fmamk_f32 v59, v130, 0xbc800000, v59
	v_fmamk_f32 v58, v130, 0xbc800000, v58
	v_fmamk_f32 v57, v130, 0xbc800000, v57
	v_fmamk_f32 v56, v130, 0xbc800000, v56
	v_fmamk_f32 v55, v130, 0xbc800000, v55
	v_fmamk_f32 v54, v130, 0xbc800000, v54
	v_fmamk_f32 v53, v130, 0xbc800000, v53
	v_fmamk_f32 v52, v130, 0xbc800000, v52
	v_fmamk_f32 v51, v130, 0xbc800000, v51
	v_fmac_f32_e32 v50, 0xbc800000, v130
	v_add_f32_dpp v66, v66, v66 row_ror:8 row_mask:0xf bank_mask:0xf bound_ctrl:1
	v_fmamk_f32 v17, v130, 0xbc800000, v17
	v_fmamk_f32 v16, v130, 0xbc800000, v16
	v_fmamk_f32 v15, v130, 0xbc800000, v15
	v_fmamk_f32 v14, v130, 0xbc800000, v14
	v_fmamk_f32 v13, v130, 0xbc800000, v13
	v_fmamk_f32 v12, v130, 0xbc800000, v12
	v_fmamk_f32 v11, v130, 0xbc800000, v11
	v_fmamk_f32 v10, v130, 0xbc800000, v10
	v_fmamk_f32 v9, v130, 0xbc800000, v9
	v_fmamk_f32 v8, v130, 0xbc800000, v8
	v_fmamk_f32 v7, v130, 0xbc800000, v7
	v_fmamk_f32 v6, v130, 0xbc800000, v6
	v_fmamk_f32 v5, v130, 0xbc800000, v5
	v_fmamk_f32 v4, v130, 0xbc800000, v4
	v_fmamk_f32 v3, v130, 0xbc800000, v3
	v_fmac_f32_e32 v2, 0xbc800000, v130
	v_pk_mul_f32 v[130:131], v[54:55], v[54:55]
	v_pk_mul_f32 v[132:133], v[62:63], v[62:63]
	v_pk_mul_f32 v[138:139], v[50:51], v[50:51]
	v_pk_mul_f32 v[140:141], v[58:59], v[58:59]
	v_pk_mul_f32 v[142:143], v[56:57], v[56:57]
	v_pk_mul_f32 v[144:145], v[64:65], v[64:65]
	v_pk_mul_f32 v[146:147], v[52:53], v[52:53]
	v_pk_mul_f32 v[148:149], v[60:61], v[60:61]
	v_mov_b32_e32 v67, v66
	v_pk_fma_f32 v[148:149], v[12:13], v[12:13], v[148:149]
	v_pk_fma_f32 v[146:147], v[4:5], v[4:5], v[146:147]
	v_pk_fma_f32 v[144:145], v[16:17], v[16:17], v[144:145]
	v_pk_fma_f32 v[142:143], v[8:9], v[8:9], v[142:143]
	v_pk_fma_f32 v[140:141], v[10:11], v[10:11], v[140:141]
	v_pk_fma_f32 v[138:139], v[2:3], v[2:3], v[138:139]
	v_pk_fma_f32 v[132:133], v[14:15], v[14:15], v[132:133]
	v_pk_fma_f32 v[130:131], v[6:7], v[6:7], v[130:131]
	v_permlane16_swap_b32_e32 v66, v67
	v_pk_add_f32 v[130:131], v[130:131], v[132:133]
	v_pk_add_f32 v[132:133], v[138:139], v[140:141]
	v_pk_add_f32 v[138:139], v[142:143], v[144:145]
	v_pk_add_f32 v[140:141], v[146:147], v[148:149]
	v_mfma_f32_32x32x16_bf16 v[18:33], v[74:77], v[78:81], v[18:33]
	v_add_f32_e32 v136, v66, v67
	ds_read_b128 v[70:73], v134 offset:512
	ds_read_b128 v[66:69], v134 offset:544
	ds_read_b128 v[78:81], v134 offset:576
	ds_read_b128 v[74:77], v134 offset:608
	ds_read_b128 v[82:85], v134 offset:640
	ds_read_b128 v[90:93], v134 offset:672
	ds_read_b128 v[86:89], v134 offset:704
	ds_read_b128 v[94:97], v134 offset:736
	v_pk_add_f32 v[138:139], v[140:141], v[138:139]
	v_pk_add_f32 v[130:131], v[132:133], v[130:131]
	s_waitcnt lgkmcnt(8)
	v_pk_mul_f32 v[140:141], v[126:127], v[62:63]
	v_pk_mov_b32 v[132:133], v[130:131], v[138:139] op_sel:[1,0]
	v_mov_b32_e32 v131, v139
	v_pk_mul_f32 v[138:139], v[122:123], v[54:55]
	v_pk_mul_f32 v[142:143], v[114:115], v[50:51]
	v_pk_mul_f32 v[144:145], v[118:119], v[58:59]
	v_pk_mul_f32 v[146:147], v[124:125], v[56:57]
	v_pk_mul_f32 v[148:149], v[128:129], v[64:65]
	v_pk_mul_f32 v[154:155], v[116:117], v[52:53]
	v_pk_mul_f32 v[156:157], v[120:121], v[60:61]
	v_pk_fma_f32 v[154:155], v[104:105], v[4:5], v[154:155]
	v_pk_fma_f32 v[156:157], v[112:113], v[12:13], v[156:157]
	v_pk_fma_f32 v[148:149], v[108:109], v[16:17], v[148:149]
	v_pk_fma_f32 v[146:147], v[100:101], v[8:9], v[146:147]
	v_pk_fma_f32 v[144:145], v[110:111], v[10:11], v[144:145]
	v_pk_fma_f32 v[142:143], v[102:103], v[2:3], v[142:143]
	v_pk_fma_f32 v[140:141], v[106:107], v[14:15], v[140:141]
	v_pk_fma_f32 v[138:139], v[98:99], v[6:7], v[138:139]
	v_pk_add_f32 v[130:131], v[132:133], v[130:131]
	v_pk_add_f32 v[138:139], v[138:139], v[140:141]
	v_pk_add_f32 v[140:141], v[142:143], v[144:145]
	v_pk_add_f32 v[142:143], v[146:147], v[148:149]
	v_pk_add_f32 v[144:145], v[154:155], v[156:157]
	v_pk_add_f32 v[132:133], v[130:131], v[130:131] op_sel:[0,1] op_sel_hi:[1,0]
	v_pk_add_f32 v[142:143], v[144:145], v[142:143]
	v_pk_add_f32 v[138:139], v[140:141], v[138:139]
	v_add_f32_e32 v133, v142, v143
	v_add_f32_e32 v130, v138, v139
	s_waitcnt lgkmcnt(2)
	v_pk_mul_f32 v[138:139], v[90:91], v[54:55]
	s_waitcnt lgkmcnt(0)
	v_pk_mul_f32 v[140:141], v[94:95], v[62:63]
	v_pk_mul_f32 v[142:143], v[82:83], v[50:51]
	v_pk_mul_f32 v[144:145], v[86:87], v[58:59]
	v_pk_mul_f32 v[146:147], v[92:93], v[56:57]
	v_pk_mul_f32 v[148:149], v[96:97], v[64:65]
	v_pk_mul_f32 v[154:155], v[84:85], v[52:53]
	v_pk_mul_f32 v[156:157], v[88:89], v[60:61]
	v_add_f32_e32 v130, v130, v133
	v_pk_fma_f32 v[156:157], v[80:81], v[12:13], v[156:157]
	v_pk_fma_f32 v[154:155], v[72:73], v[4:5], v[154:155]
	v_pk_fma_f32 v[148:149], v[76:77], v[16:17], v[148:149]
	v_pk_fma_f32 v[146:147], v[68:69], v[8:9], v[146:147]
	v_pk_fma_f32 v[144:145], v[78:79], v[10:11], v[144:145]
	v_pk_fma_f32 v[142:143], v[70:71], v[2:3], v[142:143]
	v_pk_fma_f32 v[140:141], v[74:75], v[14:15], v[140:141]
	v_pk_fma_f32 v[138:139], v[66:67], v[6:7], v[138:139]
	v_mov_b32_e32 v133, v130
	v_pk_add_f32 v[138:139], v[138:139], v[140:141]
	v_pk_add_f32 v[140:141], v[142:143], v[144:145]
	v_pk_add_f32 v[142:143], v[146:147], v[148:149]
	v_pk_add_f32 v[144:145], v[154:155], v[156:157]
	v_permlane32_swap_b32_e32 v130, v133
	v_pk_add_f32 v[142:143], v[144:145], v[142:143]
	v_add_f32_e32 v160, v130, v133
	v_pk_add_f32 v[138:139], v[140:141], v[138:139]
	v_add_f32_e32 v133, v142, v143
	v_pk_add_f32 v[140:141], v[26:27], v[42:43]
	v_pk_add_f32 v[142:143], v[28:29], v[44:45]
	v_pk_add_f32 v[144:145], v[20:21], v[36:37]
	v_pk_add_f32 v[146:147], v[32:33], v[48:49]
	v_pk_add_f32 v[148:149], v[24:25], v[40:41]
	v_pk_add_f32 v[154:155], v[30:31], v[46:47]
	v_pk_add_f32 v[156:157], v[22:23], v[38:39]
	v_pk_add_f32 v[158:159], v[18:19], v[34:35]
	v_pk_add_f32 v[154:155], v[156:157], v[154:155]
	v_pk_add_f32 v[146:147], v[148:149], v[146:147]
	v_pk_add_f32 v[142:143], v[144:145], v[142:143]
	v_pk_add_f32 v[140:141], v[158:159], v[140:141]
	v_pk_add_f32 v[142:143], v[142:143], v[146:147]
	v_pk_add_f32 v[140:141], v[140:141], v[154:155]
	v_add_f32_e32 v130, v138, v139
	v_add_f32_e32 v140, v141, v140
	v_add_f32_e32 v141, v142, v143
	v_add_f32_e32 v133, v130, v133
	v_add_f32_e32 v140, v140, v141
	v_mov_b32_e32 v131, v132
	v_mov_b32_e32 v130, v140
	s_nop 1
	v_permlane32_swap_b32_e32 v140, v130
	v_add_f32_e32 v130, v140, v130
	v_fmamk_f32 v49, v130, 0xbc800000, v49
	v_fmamk_f32 v48, v130, 0xbc800000, v48
	v_fmamk_f32 v47, v130, 0xbc800000, v47
	v_fmamk_f32 v46, v130, 0xbc800000, v46
	v_fmamk_f32 v45, v130, 0xbc800000, v45
	v_fmamk_f32 v44, v130, 0xbc800000, v44
	v_fmamk_f32 v43, v130, 0xbc800000, v43
	v_fmamk_f32 v42, v130, 0xbc800000, v42
	v_fmamk_f32 v41, v130, 0xbc800000, v41
	v_fmamk_f32 v40, v130, 0xbc800000, v40
	v_fmamk_f32 v39, v130, 0xbc800000, v39
	v_fmamk_f32 v38, v130, 0xbc800000, v38
	v_fmamk_f32 v37, v130, 0xbc800000, v37
	v_fmamk_f32 v36, v130, 0xbc800000, v36
	v_fmamk_f32 v35, v130, 0xbc800000, v35
	v_fmac_f32_e32 v34, 0xbc800000, v130
	v_fmamk_f32 v33, v130, 0xbc800000, v33
	v_fmamk_f32 v32, v130, 0xbc800000, v32
	v_fmamk_f32 v31, v130, 0xbc800000, v31
	v_fmamk_f32 v30, v130, 0xbc800000, v30
	v_fmamk_f32 v29, v130, 0xbc800000, v29
	v_fmamk_f32 v28, v130, 0xbc800000, v28
	v_fmamk_f32 v27, v130, 0xbc800000, v27
	v_fmamk_f32 v26, v130, 0xbc800000, v26
	v_fmamk_f32 v25, v130, 0xbc800000, v25
	v_fmamk_f32 v24, v130, 0xbc800000, v24
	v_fmamk_f32 v23, v130, 0xbc800000, v23
	v_fmamk_f32 v22, v130, 0xbc800000, v22
	v_fmamk_f32 v21, v130, 0xbc800000, v21
	v_fmamk_f32 v20, v130, 0xbc800000, v20
	v_fmamk_f32 v19, v130, 0xbc800000, v19
	v_fmac_f32_e32 v18, 0xbc800000, v130
	v_pk_mul_f32 v[140:141], v[38:39], v[38:39]
	v_pk_mul_f32 v[142:143], v[46:47], v[46:47]
	v_pk_mul_f32 v[144:145], v[34:35], v[34:35]
	v_pk_mul_f32 v[146:147], v[42:43], v[42:43]
	v_pk_mul_f32 v[148:149], v[40:41], v[40:41]
	v_pk_mul_f32 v[154:155], v[48:49], v[48:49]
	v_pk_mul_f32 v[156:157], v[36:37], v[36:37]
	v_pk_mul_f32 v[158:159], v[44:45], v[44:45]
	v_pk_fma_f32 v[156:157], v[20:21], v[20:21], v[156:157]
	v_pk_fma_f32 v[158:159], v[28:29], v[28:29], v[158:159]
	v_pk_fma_f32 v[154:155], v[32:33], v[32:33], v[154:155]
	v_pk_fma_f32 v[148:149], v[24:25], v[24:25], v[148:149]
	v_pk_fma_f32 v[146:147], v[26:27], v[26:27], v[146:147]
	v_pk_fma_f32 v[144:145], v[18:19], v[18:19], v[144:145]
	v_pk_fma_f32 v[142:143], v[30:31], v[30:31], v[142:143]
	v_pk_fma_f32 v[140:141], v[22:23], v[22:23], v[140:141]
	v_permlane32_swap_b32_e32 v132, v131
	v_pk_add_f32 v[140:141], v[140:141], v[142:143]
	v_pk_add_f32 v[142:143], v[144:145], v[146:147]
	v_pk_add_f32 v[144:145], v[148:149], v[154:155]
	v_pk_add_f32 v[146:147], v[156:157], v[158:159]
	v_pk_add_f32 v[140:141], v[142:143], v[140:141]
	v_pk_add_f32 v[144:145], v[146:147], v[144:145]
	v_pk_mul_f32 v[122:123], v[122:123], v[38:39]
	v_pk_mov_b32 v[142:143], v[140:141], v[144:145] op_sel:[1,0]
	v_mov_b32_e32 v141, v145
	v_pk_add_f32 v[140:141], v[142:143], v[140:141]
	v_pk_mul_f32 v[126:127], v[126:127], v[46:47]
	v_pk_add_f32 v[140:141], v[140:141], v[140:141] op_sel:[0,1] op_sel_hi:[1,0]
	v_pk_mul_f32 v[114:115], v[114:115], v[34:35]
	v_mov_b32_e32 v130, v140
	s_nop 1
	v_permlane32_swap_b32_e32 v140, v130
	v_mov_b32_e32 v141, v132
	v_pk_add_f32 v[130:131], v[140:141], v[130:131]
	v_pk_mul_f32 v[118:119], v[118:119], v[42:43]
	v_pk_fma_f32 v[130:131], v[130:131], s[0:1], v[152:153] op_sel_hi:[1,0,0]
	v_pk_mul_f32 v[124:125], v[124:125], v[40:41]
	v_pk_mul_f32 v[128:129], v[128:129], v[48:49]
	v_pk_mul_f32 v[116:117], v[116:117], v[36:37]
	v_pk_mul_f32 v[120:121], v[120:121], v[44:45]
	v_pk_fma_f32 v[112:113], v[112:113], v[28:29], v[120:121]
	v_pk_fma_f32 v[104:105], v[104:105], v[20:21], v[116:117]
	v_pk_fma_f32 v[108:109], v[108:109], v[32:33], v[128:129]
	v_pk_fma_f32 v[100:101], v[100:101], v[24:25], v[124:125]
	v_pk_fma_f32 v[110:111], v[110:111], v[26:27], v[118:119]
	v_pk_fma_f32 v[102:103], v[102:103], v[18:19], v[114:115]
	v_pk_fma_f32 v[106:107], v[106:107], v[30:31], v[126:127]
	v_pk_fma_f32 v[98:99], v[98:99], v[22:23], v[122:123]
	v_rsq_f32_e32 v131, v131
	v_pk_add_f32 v[98:99], v[98:99], v[106:107]
	v_pk_add_f32 v[102:103], v[102:103], v[110:111]
	v_pk_add_f32 v[100:101], v[100:101], v[108:109]
	v_pk_add_f32 v[104:105], v[104:105], v[112:113]
	v_rsq_f32_e32 v132, v130
	v_pk_add_f32 v[100:101], v[104:105], v[100:101]
	v_pk_add_f32 v[98:99], v[102:103], v[98:99]
	v_add_f32_e32 v98, v98, v99
	v_add_f32_e32 v99, v100, v101
	v_add_f32_e32 v98, v98, v99
	v_mov_b32_e32 v99, v98
	v_pk_mul_f32 v[90:91], v[90:91], v[38:39]
	v_pk_mul_f32 v[94:95], v[94:95], v[46:47]
	v_pk_mul_f32 v[82:83], v[82:83], v[34:35]
	v_pk_mul_f32 v[86:87], v[86:87], v[42:43]
	v_permlane32_swap_b32_e32 v98, v99
	v_pk_fma_f32 v[78:79], v[78:79], v[26:27], v[86:87]
	v_pk_fma_f32 v[70:71], v[70:71], v[18:19], v[82:83]
	v_pk_fma_f32 v[74:75], v[74:75], v[30:31], v[94:95]
	v_pk_fma_f32 v[66:67], v[66:67], v[22:23], v[90:91]
	v_mov_b32_e32 v130, v131
	v_mov_b32_e32 v131, v132
	v_add_f32_e32 v98, v98, v99
	v_pk_add_f32 v[66:67], v[66:67], v[74:75]
	v_pk_add_f32 v[70:71], v[70:71], v[78:79]
	v_mul_f32_e32 v139, v160, v130
	v_mul_f32_e32 v98, v98, v131
	v_pk_add_f32 v[66:67], v[70:71], v[66:67]
	v_cmp_gt_u32_e32 vcc, 32, v1
	v_add_f32_e32 v66, v66, v67
	v_pk_mul_f32 v[92:93], v[92:93], v[40:41]
	v_cndmask_b32_e32 v67, v98, v139, vcc
	v_add_f32_e32 v67, s12, v67
	v_pk_mul_f32 v[96:97], v[96:97], v[48:49]
	v_pk_mul_f32 v[84:85], v[84:85], v[36:37]
	v_pk_mul_f32 v[88:89], v[88:89], v[44:45]
	v_mul_f32_e32 v67, 0xbfb8aa3b, v67
	v_pk_fma_f32 v[80:81], v[80:81], v[28:29], v[88:89]
	v_pk_fma_f32 v[72:73], v[72:73], v[20:21], v[84:85]
	v_pk_fma_f32 v[76:77], v[76:77], v[32:33], v[96:97]
	v_pk_fma_f32 v[68:69], v[68:69], v[24:25], v[92:93]
	v_exp_f32_e32 v70, v67
	v_pk_add_f32 v[68:69], v[68:69], v[76:77]
	v_pk_add_f32 v[72:73], v[72:73], v[80:81]
	v_cmp_lt_i32_e64 s[0:1], 0, v151
	v_pk_add_f32 v[68:69], v[72:73], v[68:69]
	v_mov_b32_e32 v137, v136
	v_add_f32_e32 v67, v68, v69
	v_add_f32_e32 v67, v66, v67
	v_add_f32_e32 v66, 1.0, v70
	v_rcp_f32_e32 v66, v66
	v_mov_b32_e32 v69, 0xff800000
	v_mov_b32_e32 v138, v133
	v_mov_b32_e32 v68, v67
	v_cndmask_b32_e64 v70, v69, v66, s[0:1]
	v_mbcnt_lo_u32_b32 v66, -1, 0
	v_mbcnt_hi_u32_b32 v66, -1, v66
	v_permlane32_swap_b32_e32 v136, v137
	v_permlane32_swap_b32_e32 v133, v138
	v_permlane32_swap_b32_e32 v67, v68
	v_and_b32_e32 v86, 64, v66
	s_mov_b32 s14, 8
	s_mov_b32 s13, 0
	v_mov_b32_e32 v66, 0
	s_waitcnt lgkmcnt(0)
